# MLA step loop: per-step s_setprio 1/0 pair deleted (both waves of a SIMD flip together; the pair sat in the two most expensive spots)
# baseline (speedup 1.0000x reference)
.LBB0_1149:
	s_waitcnt lgkmcnt(0)
	v_mfma_f32_32x32x16_bf16 v[100:115], v[202:205], v[136:139], v[36:51]
	s_add_i32 s19, s27, -1
	s_and_b32 s18, s19, 3
	s_mul_i32 s20, s18, 0x3000
	s_and_b32 s17, s14, 0x6000
	s_add_i32 s16, s27, 2
	s_min_i32 s8, s16, s2
	s_lshl_b64 s[10:11], s[8:9], 17
	v_lshl_add_u64 v[154:155], v[176:177], 0, s[10:11]
	s_and_b32 s10, s16, 3
	s_mulk_i32 s10, 0x3000
	s_add_i32 s10, s26, s10
	s_mov_b32 m0, s10
	s_nop 0
	global_load_lds_dwordx4 v[154:155], off
	ds_read_b128 v[202:205], v156 offset:4096
	v_mfma_f32_32x32x16_bf16 v[84:99], v[190:193], v[136:139], v[36:51]
	s_and_b64 vcc, exec, s[38:39]
	s_cbranch_vccnz .Lmla_rope1
	s_lshl_b64 s[12:13], s[8:9], 18
	v_lshl_add_u64 v[154:155], v[180:181], 0, s[12:13]
	s_add_i32 m0, s10, 0x2000
	s_nop 0
	global_load_lds_dwordx4 v[154:155], off
.Lmla_rope1:
	ds_read_b128 v[190:193], v156 offset:4608
	v_mfma_f32_32x32x16_bf16 v[100:115], v[194:197], v[132:135], v[100:115]
	s_add_i32 s8, s27, 1
	s_min_i32 s8, s8, s2
	s_lshl_b32 s8, s8, 17
	v_lshl_add_u64 v[154:155], v[178:179], 0, s[8:9]
	s_add_i32 s8, s14, 0xffffe000
	s_and_b32 s15, s8, 0x6000
	s_add_i32 s8, s26, s15
	v_lshl_add_u64 v[154:155], v[154:155], 0, s[24:25]
	s_add_i32 m0, s8, 0xc000
	s_nop 0
	global_load_lds_dwordx4 v[154:155], off
	ds_read_b128 v[194:197], v156 offset:6144
	v_mfma_f32_32x32x16_bf16 v[84:99], v[198:201], v[132:135], v[84:99]
	ds_read_b128 v[198:201], v156 offset:6656
	v_exp_f32_e32 v60, v60
	v_exp_f32_e32 v61, v61
	v_exp_f32_e32 v62, v62
	v_exp_f32_e32 v63, v63
	s_waitcnt lgkmcnt(0)
	v_mfma_f32_32x32x16_bf16 v[100:115], v[202:205], v[128:131], v[100:115]
	ds_read_b128 v[202:205], v156 offset:8192
	v_exp_f32_e32 v64, v64
	v_exp_f32_e32 v65, v65
	v_exp_f32_e32 v66, v66
	v_exp_f32_e32 v67, v67
	v_mfma_f32_32x32x16_bf16 v[84:99], v[190:193], v[128:131], v[84:99]
	ds_read_b128 v[190:193], v156 offset:8704
	v_add_f32_e32 v162, v68, v69
	ds_read_b64_tr_b16 v[172:173], v157 offset:49152
	ds_read_b64_tr_b16 v[174:175], v157 offset:49664
	v_add_f32_e32 v161, v70, v162
	v_add_f32_e32 v161, v71, v161
	v_add_f32_e32 v161, v72, v161
	v_add_f32_e32 v144, v73, v161
	v_cvt_pk_bf16_f32 v140, v68, v69
	v_mfma_f32_32x32x16_bf16 v[100:115], v[194:197], v[124:127], v[100:115]
	ds_read_b128 v[194:197], v156 offset:10240
	v_cvt_pk_bf16_f32 v141, v70, v71
	ds_read_b64_tr_b16 v[68:69], v157 offset:53248
	ds_read_b64_tr_b16 v[70:71], v157 offset:53760
	v_add_f32_e32 v142, v74, v144
	v_add_f32_e32 v142, v75, v142
	v_add_f32_e32 v142, v76, v142
	v_add_f32_e32 v144, v77, v142
	v_cvt_pk_bf16_f32 v142, v72, v73
	v_mfma_f32_32x32x16_bf16 v[84:99], v[198:201], v[124:127], v[84:99]
	ds_read_b128 v[198:201], v156 offset:10752
	v_cvt_pk_bf16_f32 v143, v74, v75
	ds_read_b64_tr_b16 v[72:73], v157 offset:50176
	ds_read_b64_tr_b16 v[74:75], v157 offset:50688
	v_add_f32_e32 v144, v78, v144
	v_add_f32_e32 v144, v79, v144
	v_add_f32_e32 v144, v80, v144
	v_add_f32_e32 v148, v81, v144
	v_cvt_pk_bf16_f32 v144, v76, v77
	s_waitcnt lgkmcnt(0)
	v_mfma_f32_32x32x16_bf16 v[100:115], v[202:205], v[120:123], v[100:115]
	v_cvt_pk_bf16_f32 v145, v78, v79
	ds_read_b64_tr_b16 v[76:77], v157 offset:54272
	ds_read_b64_tr_b16 v[78:79], v157 offset:54784
	v_add_f32_e32 v146, v82, v148
	v_add_f32_e32 v146, v83, v146
	v_add_f32_e32 v146, v52, v146
	v_add_f32_e32 v148, v53, v146
	v_cvt_pk_bf16_f32 v146, v80, v81
	v_cvt_pk_bf16_f32 v147, v82, v83
	ds_read_b64_tr_b16 v[80:81], v157 offset:51200
	v_mfma_f32_32x32x16_bf16 v[84:99], v[190:193], v[120:123], v[84:99]
	ds_read_b64_tr_b16 v[82:83], v157 offset:51712
	v_add_f32_e32 v148, v54, v148
	v_add_f32_e32 v148, v55, v148
	v_add_f32_e32 v148, v56, v148
	v_add_f32_e32 v152, v57, v148
	v_cvt_pk_bf16_f32 v148, v52, v53
	v_cvt_pk_bf16_f32 v149, v54, v55
	ds_read_b64_tr_b16 v[52:53], v157 offset:55296
	ds_read_b64_tr_b16 v[54:55], v157 offset:55808
	v_add_f32_e32 v150, v58, v152
	v_mfma_f32_32x32x16_bf16 v[100:115], v[194:197], v[116:119], v[100:115]
	v_add_f32_e32 v150, v59, v150
	v_add_f32_e32 v150, v60, v150
	v_add_f32_e32 v152, v61, v150
	v_cvt_pk_bf16_f32 v150, v56, v57
	v_cvt_pk_bf16_f32 v151, v58, v59
	ds_read_b64_tr_b16 v[56:57], v157 offset:52224
	ds_read_b64_tr_b16 v[58:59], v157 offset:52736
	v_add_f32_e32 v152, v62, v152
	v_add_f32_e32 v152, v63, v152
	v_add_f32_e32 v152, v64, v152
	v_mfma_f32_32x32x16_bf16 v[84:99], v[198:201], v[116:119], v[84:99]
	v_add_f32_e32 v160, v65, v152
	v_cvt_pk_bf16_f32 v152, v60, v61
	v_cvt_pk_bf16_f32 v153, v62, v63
	ds_read_b64_tr_b16 v[60:61], v157 offset:56320
	ds_read_b64_tr_b16 v[62:63], v157 offset:56832
	v_add_f32_e32 v154, v66, v160
	v_add_f32_e32 v156, v67, v154
	v_cvt_pk_bf16_f32 v154, v64, v65
	v_cvt_pk_bf16_f32 v155, v66, v67
	s_cmp_lt_i32 s19, s52
	s_cbranch_scc0 .LBB0_1167

.LBB0_1159:
	s_waitcnt lgkmcnt(0)
	v_mfma_f32_32x32x16_bf16 v[68:83], v[202:205], v[136:139], v[36:51]
	s_add_i32 s8, s27, 3
	s_min_i32 s8, s8, s2
	s_lshl_b64 s[10:11], s[8:9], 17
	v_lshl_add_u64 v[170:171], v[176:177], 0, s[10:11]
	s_add_i32 s10, s26, s20
	s_mov_b32 m0, s10
	s_nop 0
	global_load_lds_dwordx4 v[170:171], off
	ds_read_b128 v[202:205], v140 offset:4096
	v_mfma_f32_32x32x16_bf16 v[52:67], v[190:193], v[136:139], v[36:51]
	s_and_b64 vcc, exec, s[38:39]
	s_cbranch_vccnz .Lmla_rope2
	s_lshl_b64 s[12:13], s[8:9], 18
	v_lshl_add_u64 v[170:171], v[180:181], 0, s[12:13]
	s_add_i32 m0, s10, 0x2000
	s_nop 0
	global_load_lds_dwordx4 v[170:171], off
.Lmla_rope2:
	ds_read_b128 v[190:193], v140 offset:4608
	v_mfma_f32_32x32x16_bf16 v[68:83], v[194:197], v[132:135], v[68:83]
	s_cmp_lt_u32 s19, s3
	s_cselect_b32 s8, s16, s2
	s_lshl_b64 s[10:11], s[8:9], 17
	v_lshl_add_u64 v[170:171], v[178:179], 0, s[10:11]
	s_add_i32 s8, s26, s17
	v_lshl_add_u64 v[170:171], v[170:171], 0, s[24:25]
	s_add_i32 m0, s8, 0xc000
	s_and_b32 s17, s27, 3
	global_load_lds_dwordx4 v[170:171], off
	s_mulk_i32 s17, 0x3000
	ds_read_b128 v[194:197], v140 offset:6144
	v_mfma_f32_32x32x16_bf16 v[52:67], v[198:201], v[132:135], v[52:67]
	ds_read_b128 v[198:201], v140 offset:6656
	v_exp_f32_e32 v92, v92
	v_exp_f32_e32 v93, v93
	v_exp_f32_e32 v94, v94
	v_exp_f32_e32 v95, v95
	s_waitcnt lgkmcnt(0)
	v_mfma_f32_32x32x16_bf16 v[68:83], v[202:205], v[128:131], v[68:83]
	ds_read_b128 v[202:205], v140 offset:8192
	v_exp_f32_e32 v96, v96
	v_exp_f32_e32 v97, v97
	v_exp_f32_e32 v98, v98
	v_exp_f32_e32 v99, v99
	v_mfma_f32_32x32x16_bf16 v[52:67], v[190:193], v[128:131], v[52:67]
	ds_read_b128 v[190:193], v140 offset:8704
	v_add_f32_e32 v147, v100, v101
	ds_read_b64_tr_b16 v[172:173], v141 offset:49152
	ds_read_b64_tr_b16 v[174:175], v141 offset:49664
	v_add_f32_e32 v146, v102, v147
	v_add_f32_e32 v146, v103, v146
	v_add_f32_e32 v146, v104, v146
	v_add_f32_e32 v144, v105, v146
	v_cvt_pk_bf16_f32 v156, v100, v101
	v_mfma_f32_32x32x16_bf16 v[68:83], v[194:197], v[124:127], v[68:83]
	ds_read_b128 v[194:197], v140 offset:10240
	v_cvt_pk_bf16_f32 v157, v102, v103
	ds_read_b64_tr_b16 v[100:101], v141 offset:53248
	ds_read_b64_tr_b16 v[102:103], v141 offset:53760
	v_add_f32_e32 v144, v106, v144
	v_add_f32_e32 v144, v107, v144
	v_add_f32_e32 v144, v108, v144
	v_add_f32_e32 v144, v109, v144
	v_cvt_pk_bf16_f32 v158, v104, v105
	v_mfma_f32_32x32x16_bf16 v[52:67], v[198:201], v[124:127], v[52:67]
	ds_read_b128 v[198:201], v140 offset:10752
	v_cvt_pk_bf16_f32 v159, v106, v107
	ds_read_b64_tr_b16 v[104:105], v141 offset:50176
	ds_read_b64_tr_b16 v[106:107], v141 offset:50688
	v_add_f32_e32 v144, v110, v144
	v_add_f32_e32 v144, v111, v144
	v_add_f32_e32 v144, v112, v144
	v_add_f32_e32 v144, v113, v144
	v_cvt_pk_bf16_f32 v160, v108, v109
	s_waitcnt lgkmcnt(0)
	v_mfma_f32_32x32x16_bf16 v[68:83], v[202:205], v[120:123], v[68:83]
	v_cvt_pk_bf16_f32 v161, v110, v111
	ds_read_b64_tr_b16 v[108:109], v141 offset:54272
	ds_read_b64_tr_b16 v[110:111], v141 offset:54784
	v_add_f32_e32 v144, v114, v144
	v_add_f32_e32 v144, v115, v144
	v_add_f32_e32 v144, v84, v144
	v_add_f32_e32 v144, v85, v144
	v_cvt_pk_bf16_f32 v162, v112, v113
	v_cvt_pk_bf16_f32 v163, v114, v115
	ds_read_b64_tr_b16 v[112:113], v141 offset:51200
	v_mfma_f32_32x32x16_bf16 v[52:67], v[190:193], v[120:123], v[52:67]
	ds_read_b64_tr_b16 v[114:115], v141 offset:51712
	v_add_f32_e32 v144, v86, v144
	v_add_f32_e32 v144, v87, v144
	v_add_f32_e32 v144, v88, v144
	v_add_f32_e32 v144, v89, v144
	v_cvt_pk_bf16_f32 v164, v84, v85
	v_cvt_pk_bf16_f32 v165, v86, v87
	ds_read_b64_tr_b16 v[84:85], v141 offset:55296
	ds_read_b64_tr_b16 v[86:87], v141 offset:55808
	v_add_f32_e32 v144, v90, v144
	v_mfma_f32_32x32x16_bf16 v[68:83], v[194:197], v[116:119], v[68:83]
	v_add_f32_e32 v144, v91, v144
	v_add_f32_e32 v144, v92, v144
	v_add_f32_e32 v144, v93, v144
	v_cvt_pk_bf16_f32 v166, v88, v89
	v_cvt_pk_bf16_f32 v167, v90, v91
	ds_read_b64_tr_b16 v[88:89], v141 offset:52224
	ds_read_b64_tr_b16 v[90:91], v141 offset:52736
	v_add_f32_e32 v144, v94, v144
	v_add_f32_e32 v144, v95, v144
	v_add_f32_e32 v144, v96, v144
	v_mfma_f32_32x32x16_bf16 v[52:67], v[198:201], v[116:119], v[52:67]
	v_add_f32_e32 v144, v97, v144
	v_cvt_pk_bf16_f32 v168, v92, v93
	v_cvt_pk_bf16_f32 v169, v94, v95
	ds_read_b64_tr_b16 v[92:93], v141 offset:56320
	ds_read_b64_tr_b16 v[94:95], v141 offset:56832
	v_add_f32_e32 v140, v98, v144
	v_add_f32_e32 v140, v99, v140
	v_cvt_pk_bf16_f32 v170, v96, v97
	v_cvt_pk_bf16_f32 v171, v98, v99
	s_cmp_lt_i32 s27, s52
	s_cbranch_scc0 .LBB0_1171
